# LH router: the eight partial-logit LDS reads per token issued together into spare registers with counted waits (same adds, same order)
# speedup vs baseline: 1.0131x; 1.0026x over previous
; #define LAS __attribute__((address_space(3)))
; __global__ void __launch_bounds__(NWAVES * 64, 2) fwd(Args args) {
;     ...
;                     for (int tk = 0; tk < 2; ++tk) { float cur[4] = {be4[0], be4[1], be4[2], be4[3]};
; #pragma unroll
;                         for (int w = 0; w < 8; ++w) { const f32x4 p = *(const LAS f32x4*)(part + (w * 16 + 2 * wave + tk) * 32 + 4 * eq);
; #pragma unroll
;                             for (int j = 0; j < 4; ++j) cur[j] += p[j]; }
;                         float val[4]; int idx[4];
; #pragma unroll
;                         for (int k = 0; k < 4; ++k) { float bv = cur[0]; int bi = 4 * eq;
; #pragma unroll
;                             for (int j = 1; j < 4; ++j) if (cur[j] > bv) { bv = cur[j]; bi = 4 * eq + j; }
.LBB0_3070:
	s_or_b32 s12, s35, s46
	v_lshl_add_u32 v134, s12, 7, v141
	ds_read_b128 v[170:173], v134
	ds_read_b128 v[174:177], v134 offset:2048
	ds_read_b128 v[178:181], v134 offset:4096
	ds_read_b128 v[182:185], v134 offset:6144
	ds_read_b128 v[186:189], v134 offset:8192
	ds_read_b128 v[190:193], v134 offset:10240
	ds_read_b128 v[194:197], v134 offset:12288
	ds_read_b128 v[198:201], v134 offset:14336
	s_waitcnt vmcnt(0) lgkmcnt(7)
	v_add_f32_e32 v135, v172, v98
	v_add_f32_e32 v139, v173, v99
	s_waitcnt lgkmcnt(6)
	v_add_f32_e32 v135, v176, v135
	v_add_f32_e32 v139, v177, v139
	s_waitcnt lgkmcnt(5)
	v_add_f32_e32 v135, v180, v135
	v_add_f32_e32 v139, v181, v139
	s_waitcnt lgkmcnt(4)
	v_add_f32_e32 v135, v184, v135
	v_add_f32_e32 v139, v185, v139
	s_waitcnt lgkmcnt(3)
	v_add_f32_e32 v135, v188, v135
	v_add_f32_e32 v139, v189, v139
	s_waitcnt lgkmcnt(2)
	v_add_f32_e32 v135, v192, v135
	v_add_f32_e32 v139, v193, v139
	s_waitcnt lgkmcnt(1)
	v_add_f32_e32 v168, v196, v135
	v_add_f32_e32 v139, v197, v139
	v_pk_add_f32 v[134:135], v[170:171], v[96:97]
	s_waitcnt lgkmcnt(0)
	v_add_f32_e32 v151, v201, v139
	v_pk_add_f32 v[134:135], v[174:175], v[134:135]
	v_add_f32_e32 v152, v200, v168
	v_pk_add_f32 v[134:135], v[178:179], v[134:135]
	s_nop 0
	v_pk_add_f32 v[134:135], v[182:183], v[134:135]
	s_nop 0
	v_pk_add_f32 v[134:135], v[186:187], v[134:135]
	s_nop 0
	v_pk_add_f32 v[134:135], v[190:191], v[134:135]
	s_nop 0
	v_pk_add_f32 v[134:135], v[194:195], v[134:135]
	s_nop 0
	v_pk_add_f32 v[134:135], v[198:199], v[134:135]
	s_nop 0
	v_cmp_gt_f32_e32 vcc, v135, v134
	s_nop 1
	v_cndmask_b32_e32 v150, v134, v135, vcc
	v_cndmask_b32_e32 v139, v106, v101, vcc
	v_cmp_gt_f32_e32 vcc, v152, v150
	s_nop 1
	v_cndmask_b32_e32 v150, v150, v152, vcc
	v_cndmask_b32_e32 v139, v139, v145, vcc
	v_cmp_gt_f32_e32 vcc, v151, v150
	s_nop 1
	v_cndmask_b32_e32 v150, v150, v151, vcc
	v_cndmask_b32_e32 v139, v139, v146, vcc
	s_nop 1
	v_mov_b32_dpp v153, v150 quad_perm:[1,0,3,2] row_mask:0xf bank_mask:0xf
	s_nop 1
	v_mov_b32_dpp v154, v139 quad_perm:[1,0,3,2] row_mask:0xf bank_mask:0xf
	s_waitcnt lgkmcnt(1)
	v_cmp_lt_f32_e64 s[24:25], v150, v153
	v_cmp_nlt_f32_e32 vcc, v150, v153
	s_and_saveexec_b64 s[26:27], vcc
	s_cbranch_execz .LBB0_3072
	v_cmp_eq_f32_e32 vcc, v150, v153
	s_waitcnt lgkmcnt(0)
	v_cmp_lt_i32_e64 s[12:13], v154, v139
	s_and_b64 s[12:13], vcc, s[12:13]
	s_andn2_b64 s[24:25], s[24:25], exec
	s_and_b64 s[12:13], s[12:13], exec
	s_or_b64 s[24:25], s[24:25], s[12:13]
